# speedup vs baseline: 1.0262x; 1.0025x over previous
.LBB1_82:
	ds_read_b128 v[130:133], v219 offset:32768
	ds_read_b128 v[134:137], v219 offset:33792
	ds_read_b128 v[138:141], v219 offset:34816
	ds_read_b128 v[142:145], v219 offset:35840
	ds_read_b128 v[178:181], v219 offset:49152
	ds_read_b128 v[182:185], v219 offset:50176
	ds_read_b128 v[186:189], v219 offset:51200
	ds_read_b128 v[190:193], v219 offset:52224
	ds_read_b128 v[146:149], v220
	ds_read_b128 v[150:153], v220 offset:1024
	ds_read_b128 v[154:157], v221
	ds_read_b128 v[158:161], v221 offset:1024
	ds_read_b128 v[162:165], v222
	ds_read_b128 v[166:169], v222 offset:1024
	ds_read_b128 v[170:173], v223
	ds_read_b128 v[174:177], v223 offset:1024
	s_add_i32 s12, s8, 1
	s_mov_b32 m0, s43
	v_readlane_b32 s9, v248, s12
	s_nop 1
	v_add_u32_e32 v251, s9, v249
	global_load_lds_dwordx4 v251, s[18:19]
	v_add_u32_e32 v251, s9, v250
	s_mov_b32 m0, s44
	s_nop 0
	global_load_lds_dwordx4 v251, s[18:19]
	s_waitcnt vmcnt(8) lgkmcnt(0)
	s_barrier
	v_mfma_f32_16x16x32_f16 v[124:127], v[130:133], v[146:149], v[124:127]
	v_mfma_f32_16x16x32_f16 v[124:127], v[134:137], v[150:153], v[124:127]
	v_mfma_f32_16x16x32_f16 v[120:123], v[138:141], v[146:149], v[120:123]
	v_mfma_f32_16x16x32_f16 v[120:123], v[142:145], v[150:153], v[120:123]
	v_mfma_f32_16x16x32_f16 v[52:55], v[178:181], v[146:149], v[52:55]
	v_mfma_f32_16x16x32_f16 v[52:55], v[182:185], v[150:153], v[52:55]
	v_mfma_f32_16x16x32_f16 v[40:43], v[186:189], v[146:149], v[40:43]
	v_mfma_f32_16x16x32_f16 v[40:43], v[190:193], v[150:153], v[40:43]
	v_mfma_f32_16x16x32_f16 v[32:35], v[186:189], v[154:157], v[32:35]
	v_mfma_f32_16x16x32_f16 v[32:35], v[190:193], v[158:161], v[32:35]
	v_mfma_f32_16x16x32_f16 v[36:39], v[178:181], v[154:157], v[36:39]
	v_mfma_f32_16x16x32_f16 v[36:39], v[182:185], v[158:161], v[36:39]
	v_mfma_f32_16x16x32_f16 v[112:115], v[138:141], v[154:157], v[112:115]
	v_mfma_f32_16x16x32_f16 v[112:115], v[142:145], v[158:161], v[112:115]
	v_mfma_f32_16x16x32_f16 v[116:119], v[130:133], v[154:157], v[116:119]
	v_mfma_f32_16x16x32_f16 v[116:119], v[134:137], v[158:161], v[116:119]
	v_mfma_f32_16x16x32_f16 v[108:111], v[130:133], v[162:165], v[108:111]
	v_mfma_f32_16x16x32_f16 v[108:111], v[134:137], v[166:169], v[108:111]
	v_mfma_f32_16x16x32_f16 v[104:107], v[138:141], v[162:165], v[104:107]
	v_mfma_f32_16x16x32_f16 v[104:107], v[142:145], v[166:169], v[104:107]
	v_mfma_f32_16x16x32_f16 v[28:31], v[178:181], v[162:165], v[28:31]
	v_mfma_f32_16x16x32_f16 v[28:31], v[182:185], v[166:169], v[28:31]
	v_mfma_f32_16x16x32_f16 v[24:27], v[186:189], v[162:165], v[24:27]
	v_mfma_f32_16x16x32_f16 v[24:27], v[190:193], v[166:169], v[24:27]
	v_mfma_f32_16x16x32_f16 v[16:19], v[186:189], v[170:173], v[16:19]
	v_mfma_f32_16x16x32_f16 v[16:19], v[190:193], v[174:177], v[16:19]
	v_mfma_f32_16x16x32_f16 v[20:23], v[178:181], v[170:173], v[20:23]
	v_mfma_f32_16x16x32_f16 v[20:23], v[182:185], v[174:177], v[20:23]
	v_mfma_f32_16x16x32_f16 v[96:99], v[138:141], v[170:173], v[96:99]
	v_mfma_f32_16x16x32_f16 v[96:99], v[142:145], v[174:177], v[96:99]
	v_mfma_f32_16x16x32_f16 v[100:103], v[130:133], v[170:173], v[100:103]
	v_mfma_f32_16x16x32_f16 v[100:103], v[134:137], v[174:177], v[100:103]
	s_barrier
	ds_read_b128 v[146:149], v220 offset:16384
	ds_read_b128 v[150:153], v220 offset:17408
	ds_read_b128 v[154:157], v221 offset:16384
	ds_read_b128 v[158:161], v221 offset:17408
	ds_read_b128 v[162:165], v222 offset:16384
	ds_read_b128 v[166:169], v222 offset:17408
	ds_read_b128 v[170:173], v223 offset:16384
	ds_read_b128 v[174:177], v223 offset:17408
	v_add_u32_e32 v129, s7, v128
	s_mov_b32 m0, s22
	v_add_u32_e32 v194, 0xffffff80, v129
	global_load_lds_dwordx4 v194, s[10:11]
	v_add_u32_e32 v194, 0x47f80, v129
	s_mov_b32 m0, s23
	s_add_i32 s9, s8, 2
	global_load_lds_dwordx4 v194, s[10:11]
	v_readlane_b32 s13, v248, s9
	s_mov_b32 m0, s21
	s_nop 1
	v_add_u32_e32 v194, s13, v206
	global_load_lds_dwordx4 v194, s[18:19]
	v_add_u32_e32 v194, s13, v213
	s_mov_b32 m0, s24
	s_nop 0
	global_load_lds_dwordx4 v194, s[18:19]
	s_mov_b32 m0, s25
	v_add_u32_e32 v194, 0x8ff80, v129
	global_load_lds_dwordx4 v194, s[10:11]
	v_add_u32_e32 v194, 0xd7f80, v129
	s_mov_b32 m0, s26
	s_nop 0
	global_load_lds_dwordx4 v194, s[10:11]
	s_waitcnt vmcnt(8) lgkmcnt(0)
	s_barrier
	v_mfma_f32_16x16x32_f16 v[12:15], v[130:133], v[146:149], v[12:15]
	v_mfma_f32_16x16x32_f16 v[12:15], v[134:137], v[150:153], v[12:15]
	v_mfma_f32_16x16x32_f16 v[8:11], v[138:141], v[146:149], v[8:11]
	v_mfma_f32_16x16x32_f16 v[8:11], v[142:145], v[150:153], v[8:11]
	v_mfma_f32_16x16x32_f16 v[64:67], v[178:181], v[146:149], v[64:67]
	v_mfma_f32_16x16x32_f16 v[64:67], v[182:185], v[150:153], v[64:67]
	v_mfma_f32_16x16x32_f16 v[68:71], v[186:189], v[146:149], v[68:71]
	v_mfma_f32_16x16x32_f16 v[68:71], v[190:193], v[150:153], v[68:71]
	v_mfma_f32_16x16x32_f16 v[76:79], v[186:189], v[154:157], v[76:79]
	v_mfma_f32_16x16x32_f16 v[76:79], v[190:193], v[158:161], v[76:79]
	v_mfma_f32_16x16x32_f16 v[72:75], v[178:181], v[154:157], v[72:75]
	v_mfma_f32_16x16x32_f16 v[72:75], v[182:185], v[158:161], v[72:75]
	v_mfma_f32_16x16x32_f16 v[0:3], v[138:141], v[154:157], v[0:3]
	v_mfma_f32_16x16x32_f16 v[0:3], v[142:145], v[158:161], v[0:3]
	v_mfma_f32_16x16x32_f16 v[4:7], v[130:133], v[154:157], v[4:7]
	v_mfma_f32_16x16x32_f16 v[4:7], v[134:137], v[158:161], v[4:7]
	v_mfma_f32_16x16x32_f16 v[44:47], v[130:133], v[162:165], v[44:47]
	v_mfma_f32_16x16x32_f16 v[44:47], v[134:137], v[166:169], v[44:47]
	v_mfma_f32_16x16x32_f16 v[48:51], v[138:141], v[162:165], v[48:51]
	v_mfma_f32_16x16x32_f16 v[48:51], v[142:145], v[166:169], v[48:51]
	v_mfma_f32_16x16x32_f16 v[80:83], v[178:181], v[162:165], v[80:83]
	v_mfma_f32_16x16x32_f16 v[80:83], v[182:185], v[166:169], v[80:83]
	v_mfma_f32_16x16x32_f16 v[84:87], v[186:189], v[162:165], v[84:87]
	v_mfma_f32_16x16x32_f16 v[84:87], v[190:193], v[166:169], v[84:87]
	v_mfma_f32_16x16x32_f16 v[92:95], v[186:189], v[170:173], v[92:95]
	v_mfma_f32_16x16x32_f16 v[92:95], v[190:193], v[174:177], v[92:95]
	v_mfma_f32_16x16x32_f16 v[88:91], v[178:181], v[170:173], v[88:91]
	v_mfma_f32_16x16x32_f16 v[88:91], v[182:185], v[174:177], v[88:91]
	v_mfma_f32_16x16x32_f16 v[60:63], v[138:141], v[170:173], v[60:63]
	v_mfma_f32_16x16x32_f16 v[60:63], v[142:145], v[174:177], v[60:63]
	v_mfma_f32_16x16x32_f16 v[56:59], v[130:133], v[170:173], v[56:59]
	v_mfma_f32_16x16x32_f16 v[56:59], v[134:137], v[174:177], v[56:59]
	s_barrier
	ds_read_b128 v[130:133], v224
	ds_read_b128 v[134:137], v224 offset:1024
	ds_read_b128 v[138:141], v224 offset:2048
	ds_read_b128 v[142:145], v224 offset:3072
	ds_read_b128 v[178:181], v229
	ds_read_b128 v[182:185], v229 offset:1024
	ds_read_b128 v[186:189], v229 offset:2048
	ds_read_b128 v[190:193], v229 offset:3072
	ds_read_b128 v[146:149], v225
	ds_read_b128 v[150:153], v225 offset:1024
	ds_read_b128 v[154:157], v226
	ds_read_b128 v[158:161], v226 offset:1024
	ds_read_b128 v[162:165], v227
	ds_read_b128 v[166:169], v227 offset:1024
	ds_read_b128 v[170:173], v228
	ds_read_b128 v[174:177], v228 offset:1024
	v_readlane_b32 s12, v248, s9
	s_mov_b32 m0, s27
	s_nop 1
	v_add_u32_e32 v251, s12, v249
	global_load_lds_dwordx4 v251, s[18:19]
	s_mov_b32 m0, s28
	v_add_u32_e32 v251, s12, v250
	global_load_lds_dwordx4 v251, s[18:19]
	s_waitcnt vmcnt(8) lgkmcnt(0)
	s_barrier
	v_mfma_f32_16x16x32_f16 v[124:127], v[130:133], v[146:149], v[124:127]
	v_mfma_f32_16x16x32_f16 v[124:127], v[134:137], v[150:153], v[124:127]
	v_mfma_f32_16x16x32_f16 v[120:123], v[138:141], v[146:149], v[120:123]
	v_mfma_f32_16x16x32_f16 v[120:123], v[142:145], v[150:153], v[120:123]
	v_mfma_f32_16x16x32_f16 v[52:55], v[178:181], v[146:149], v[52:55]
	v_mfma_f32_16x16x32_f16 v[52:55], v[182:185], v[150:153], v[52:55]
	v_mfma_f32_16x16x32_f16 v[40:43], v[186:189], v[146:149], v[40:43]
	v_mfma_f32_16x16x32_f16 v[40:43], v[190:193], v[150:153], v[40:43]
	v_mfma_f32_16x16x32_f16 v[32:35], v[186:189], v[154:157], v[32:35]
	v_mfma_f32_16x16x32_f16 v[32:35], v[190:193], v[158:161], v[32:35]
	v_mfma_f32_16x16x32_f16 v[36:39], v[178:181], v[154:157], v[36:39]
	v_mfma_f32_16x16x32_f16 v[36:39], v[182:185], v[158:161], v[36:39]
	v_mfma_f32_16x16x32_f16 v[112:115], v[138:141], v[154:157], v[112:115]
	v_mfma_f32_16x16x32_f16 v[112:115], v[142:145], v[158:161], v[112:115]
	v_mfma_f32_16x16x32_f16 v[116:119], v[130:133], v[154:157], v[116:119]
	v_mfma_f32_16x16x32_f16 v[116:119], v[134:137], v[158:161], v[116:119]
	v_mfma_f32_16x16x32_f16 v[108:111], v[130:133], v[162:165], v[108:111]
	v_mfma_f32_16x16x32_f16 v[108:111], v[134:137], v[166:169], v[108:111]
	v_mfma_f32_16x16x32_f16 v[104:107], v[138:141], v[162:165], v[104:107]
	v_mfma_f32_16x16x32_f16 v[104:107], v[142:145], v[166:169], v[104:107]
	v_mfma_f32_16x16x32_f16 v[28:31], v[178:181], v[162:165], v[28:31]
	v_mfma_f32_16x16x32_f16 v[28:31], v[182:185], v[166:169], v[28:31]
	v_mfma_f32_16x16x32_f16 v[24:27], v[186:189], v[162:165], v[24:27]
	v_mfma_f32_16x16x32_f16 v[24:27], v[190:193], v[166:169], v[24:27]
	v_mfma_f32_16x16x32_f16 v[16:19], v[186:189], v[170:173], v[16:19]
	v_mfma_f32_16x16x32_f16 v[16:19], v[190:193], v[174:177], v[16:19]
	v_mfma_f32_16x16x32_f16 v[20:23], v[178:181], v[170:173], v[20:23]
	v_mfma_f32_16x16x32_f16 v[20:23], v[182:185], v[174:177], v[20:23]
	v_mfma_f32_16x16x32_f16 v[96:99], v[138:141], v[170:173], v[96:99]
	v_mfma_f32_16x16x32_f16 v[96:99], v[142:145], v[174:177], v[96:99]
	v_mfma_f32_16x16x32_f16 v[100:103], v[130:133], v[170:173], v[100:103]
	v_mfma_f32_16x16x32_f16 v[100:103], v[134:137], v[174:177], v[100:103]
	s_barrier
	ds_read_b128 v[146:149], v230
	ds_read_b128 v[150:153], v230 offset:1024
	ds_read_b128 v[154:157], v231
	ds_read_b128 v[158:161], v231 offset:1024
	ds_read_b128 v[162:165], v232
	ds_read_b128 v[166:169], v232 offset:1024
	ds_read_b128 v[170:173], v233
	ds_read_b128 v[174:177], v233 offset:1024
	s_mov_b32 m0, s37
	v_add_u32_e32 v194, 0x48000, v129
	global_load_lds_dwordx4 v129, s[10:11]
	s_mov_b32 m0, s38
	s_add_i32 s12, s8, 3
	global_load_lds_dwordx4 v194, s[10:11]
	v_readlane_b32 s13, v248, s12
	s_mov_b32 m0, s39
	s_nop 1
	v_add_u32_e32 v194, s13, v206
	global_load_lds_dwordx4 v194, s[18:19]
	s_mov_b32 m0, s40
	v_add_u32_e32 v194, s13, v213
	global_load_lds_dwordx4 v194, s[18:19]
	s_mov_b32 m0, s41
	v_add_u32_e32 v194, 0x90000, v129
	global_load_lds_dwordx4 v194, s[10:11]
	v_add_u32_e32 v194, 0xd8000, v129
	s_mov_b32 m0, s42
	s_nop 0
	global_load_lds_dwordx4 v194, s[10:11]
	s_waitcnt vmcnt(8) lgkmcnt(0)
	s_barrier
	v_mfma_f32_16x16x32_f16 v[12:15], v[130:133], v[146:149], v[12:15]
	v_mfma_f32_16x16x32_f16 v[12:15], v[134:137], v[150:153], v[12:15]
	v_mfma_f32_16x16x32_f16 v[8:11], v[138:141], v[146:149], v[8:11]
	v_mfma_f32_16x16x32_f16 v[8:11], v[142:145], v[150:153], v[8:11]
	v_mfma_f32_16x16x32_f16 v[64:67], v[178:181], v[146:149], v[64:67]
	v_mfma_f32_16x16x32_f16 v[64:67], v[182:185], v[150:153], v[64:67]
	v_mfma_f32_16x16x32_f16 v[68:71], v[186:189], v[146:149], v[68:71]
	v_mfma_f32_16x16x32_f16 v[68:71], v[190:193], v[150:153], v[68:71]
	v_mfma_f32_16x16x32_f16 v[76:79], v[186:189], v[154:157], v[76:79]
	v_mfma_f32_16x16x32_f16 v[76:79], v[190:193], v[158:161], v[76:79]
	v_mfma_f32_16x16x32_f16 v[72:75], v[178:181], v[154:157], v[72:75]
	v_mfma_f32_16x16x32_f16 v[72:75], v[182:185], v[158:161], v[72:75]
	v_mfma_f32_16x16x32_f16 v[0:3], v[138:141], v[154:157], v[0:3]
	v_mfma_f32_16x16x32_f16 v[0:3], v[142:145], v[158:161], v[0:3]
	v_mfma_f32_16x16x32_f16 v[4:7], v[130:133], v[154:157], v[4:7]
	v_mfma_f32_16x16x32_f16 v[4:7], v[134:137], v[158:161], v[4:7]
	v_mfma_f32_16x16x32_f16 v[44:47], v[130:133], v[162:165], v[44:47]
	v_mfma_f32_16x16x32_f16 v[44:47], v[134:137], v[166:169], v[44:47]
	v_mfma_f32_16x16x32_f16 v[48:51], v[138:141], v[162:165], v[48:51]
	v_mfma_f32_16x16x32_f16 v[48:51], v[142:145], v[166:169], v[48:51]
	v_mfma_f32_16x16x32_f16 v[80:83], v[178:181], v[162:165], v[80:83]
	v_mfma_f32_16x16x32_f16 v[80:83], v[182:185], v[166:169], v[80:83]
	v_mfma_f32_16x16x32_f16 v[84:87], v[186:189], v[162:165], v[84:87]
	v_mfma_f32_16x16x32_f16 v[84:87], v[190:193], v[166:169], v[84:87]
	v_mfma_f32_16x16x32_f16 v[92:95], v[186:189], v[170:173], v[92:95]
	v_mfma_f32_16x16x32_f16 v[92:95], v[190:193], v[174:177], v[92:95]
	v_mfma_f32_16x16x32_f16 v[88:91], v[178:181], v[170:173], v[88:91]
	v_mfma_f32_16x16x32_f16 v[88:91], v[182:185], v[174:177], v[88:91]
	v_mfma_f32_16x16x32_f16 v[60:63], v[138:141], v[170:173], v[60:63]
	v_mfma_f32_16x16x32_f16 v[60:63], v[142:145], v[174:177], v[60:63]
	v_mfma_f32_16x16x32_f16 v[56:59], v[130:133], v[170:173], v[56:59]
	v_mfma_f32_16x16x32_f16 v[56:59], v[134:137], v[174:177], v[56:59]
	s_addk_i32 s7, 0x100
	s_cmp_lt_u32 s8, 32
	s_mov_b32 s8, s9
	s_barrier
	s_cbranch_scc1 .LBB1_82
	ds_read_b128 v[132:135], v219 offset:32768
	ds_read_b128 v[136:139], v219 offset:33792
	ds_read_b128 v[140:143], v219 offset:34816
	ds_read_b128 v[144:147], v219 offset:35840
	ds_read_b128 v[128:131], v220
	ds_read_b128 v[148:151], v220 offset:1024
	ds_read_b128 v[152:155], v221
	ds_read_b128 v[156:159], v221 offset:1024
	ds_read_b128 v[188:191], v222
	ds_read_b128 v[192:195], v222 offset:1024
	ds_read_b128 v[196:199], v223
	ds_read_b128 v[200:203], v223 offset:1024
	s_setprio 2
	s_lshl_b32 s3, s50, 9
	s_add_i32 s3, s47, s3
	s_add_i32 s3, s3, 0x10380
	s_mov_b32 m0, s43
	v_add_u32_e32 v160, s3, v206
	global_load_lds_dwordx4 v160, s[18:19]
	v_add_u32_e32 v160, s3, v213
	s_mov_b32 m0, s44
	s_nop 0
	global_load_lds_dwordx4 v160, s[18:19]
	s_setprio 0
	s_waitcnt vmcnt(8)
	s_waitcnt lgkmcnt(0)
	s_barrier
	s_waitcnt lgkmcnt(0)
	s_setprio 1
	s_waitcnt lgkmcnt(0)
	v_mfma_f32_16x16x32_f16 v[124:127], v[132:135], v[128:131], v[124:127]
	v_mfma_f32_16x16x32_f16 v[120:123], v[140:143], v[128:131], v[120:123]
	v_mfma_f32_16x16x32_f16 v[116:119], v[132:135], v[152:155], v[116:119]
	v_mfma_f32_16x16x32_f16 v[112:115], v[140:143], v[152:155], v[112:115]
	v_mfma_f32_16x16x32_f16 v[108:111], v[132:135], v[188:191], v[108:111]
	v_mfma_f32_16x16x32_f16 v[104:107], v[140:143], v[188:191], v[104:107]
	v_mfma_f32_16x16x32_f16 v[100:103], v[132:135], v[196:199], v[100:103]
	v_mfma_f32_16x16x32_f16 v[96:99], v[140:143], v[196:199], v[96:99]
	v_mfma_f32_16x16x32_f16 v[160:163], v[136:139], v[148:151], v[124:127]
	v_mfma_f32_16x16x32_f16 v[164:167], v[144:147], v[148:151], v[120:123]
	v_mfma_f32_16x16x32_f16 v[168:171], v[136:139], v[156:159], v[116:119]
	v_mfma_f32_16x16x32_f16 v[172:175], v[144:147], v[156:159], v[112:115]
	v_mfma_f32_16x16x32_f16 v[176:179], v[136:139], v[192:195], v[108:111]
	v_mfma_f32_16x16x32_f16 v[180:183], v[144:147], v[192:195], v[104:107]
	v_mfma_f32_16x16x32_f16 v[100:103], v[136:139], v[200:203], v[100:103]
	v_mfma_f32_16x16x32_f16 v[184:187], v[144:147], v[200:203], v[96:99]
	s_setprio 0
	s_barrier
	ds_read_b128 v[104:107], v219 offset:49152
	ds_read_b128 v[108:111], v219 offset:50176
	ds_read_b128 v[116:119], v219 offset:51200
	ds_read_b128 v[236:239], v219 offset:52224
	s_waitcnt lgkmcnt(0)
	s_barrier
	s_waitcnt lgkmcnt(0)
	s_setprio 1
	s_waitcnt lgkmcnt(0)
	v_mfma_f32_16x16x32_f16 v[52:55], v[104:107], v[128:131], v[52:55]
	v_mfma_f32_16x16x32_f16 v[40:43], v[116:119], v[128:131], v[40:43]
	v_mfma_f32_16x16x32_f16 v[36:39], v[104:107], v[152:155], v[36:39]
	v_mfma_f32_16x16x32_f16 v[32:35], v[116:119], v[152:155], v[32:35]
	v_mfma_f32_16x16x32_f16 v[28:31], v[104:107], v[188:191], v[28:31]
	v_mfma_f32_16x16x32_f16 v[24:27], v[116:119], v[188:191], v[24:27]
	v_mfma_f32_16x16x32_f16 v[20:23], v[104:107], v[196:199], v[20:23]
	v_mfma_f32_16x16x32_f16 v[16:19], v[116:119], v[196:199], v[16:19]
	v_mfma_f32_16x16x32_f16 v[52:55], v[108:111], v[148:151], v[52:55]
	v_mfma_f32_16x16x32_f16 v[40:43], v[236:239], v[148:151], v[40:43]
	v_mfma_f32_16x16x32_f16 v[36:39], v[108:111], v[156:159], v[36:39]
	v_mfma_f32_16x16x32_f16 v[32:35], v[236:239], v[156:159], v[32:35]
	v_mfma_f32_16x16x32_f16 v[28:31], v[108:111], v[192:195], v[28:31]
	v_mfma_f32_16x16x32_f16 v[24:27], v[236:239], v[192:195], v[24:27]
	v_mfma_f32_16x16x32_f16 v[96:99], v[108:111], v[200:203], v[20:23]
	v_mfma_f32_16x16x32_f16 v[16:19], v[236:239], v[200:203], v[16:19]
	s_setprio 0
	s_barrier
	ds_read_b128 v[20:23], v220 offset:16384
	ds_read_b128 v[148:151], v220 offset:17408
	ds_read_b128 v[152:155], v221 offset:16384
	ds_read_b128 v[156:159], v221 offset:17408
	ds_read_b128 v[188:191], v222 offset:16384
	ds_read_b128 v[192:195], v222 offset:17408
	ds_read_b128 v[196:199], v223 offset:16384
	ds_read_b128 v[200:203], v223 offset:17408
	s_waitcnt vmcnt(4)
	s_waitcnt lgkmcnt(0)
	s_barrier
	s_waitcnt lgkmcnt(0)
	s_setprio 1
	s_waitcnt lgkmcnt(0)
	v_mfma_f32_16x16x32_f16 v[0:3], v[140:143], v[152:155], v[0:3]
	v_mfma_f32_16x16x32_f16 v[124:127], v[144:147], v[156:159], v[0:3]
	v_mfma_f32_16x16x32_f16 v[0:3], v[132:135], v[188:191], v[44:47]
	v_mfma_f32_16x16x32_f16 v[128:131], v[136:139], v[192:195], v[0:3]
	v_mfma_f32_16x16x32_f16 v[0:3], v[140:143], v[188:191], v[48:51]
	v_mfma_f32_16x16x32_f16 v[48:51], v[144:147], v[192:195], v[0:3]
	v_mfma_f32_16x16x32_f16 v[0:3], v[132:135], v[196:199], v[56:59]
	v_mfma_f32_16x16x32_f16 v[12:15], v[132:135], v[20:23], v[12:15]
	v_mfma_f32_16x16x32_f16 v[8:11], v[140:143], v[20:23], v[8:11]
	v_mfma_f32_16x16x32_f16 v[4:7], v[132:135], v[152:155], v[4:7]
	v_mfma_f32_16x16x32_f16 v[56:59], v[136:139], v[200:203], v[0:3]
	v_mfma_f32_16x16x32_f16 v[0:3], v[140:143], v[196:199], v[60:63]
	v_mfma_f32_16x16x32_f16 v[112:115], v[136:139], v[148:151], v[12:15]
	v_mfma_f32_16x16x32_f16 v[8:11], v[144:147], v[148:151], v[8:11]
	v_mfma_f32_16x16x32_f16 v[120:123], v[136:139], v[156:159], v[4:7]
	v_mfma_f32_16x16x32_f16 v[60:63], v[144:147], v[200:203], v[0:3]
	s_setprio 0
	s_setprio 1
	v_mfma_f32_16x16x32_f16 v[0:3], v[104:107], v[20:23], v[64:67]
	v_mfma_f32_16x16x32_f16 v[132:135], v[108:111], v[148:151], v[0:3]
	v_mfma_f32_16x16x32_f16 v[0:3], v[116:119], v[20:23], v[68:71]
	v_mfma_f32_16x16x32_f16 v[136:139], v[236:239], v[148:151], v[0:3]
	v_mfma_f32_16x16x32_f16 v[0:3], v[104:107], v[152:155], v[72:75]
	v_mfma_f32_16x16x32_f16 v[140:143], v[108:111], v[156:159], v[0:3]
	v_mfma_f32_16x16x32_f16 v[0:3], v[116:119], v[152:155], v[76:79]
	v_mfma_f32_16x16x32_f16 v[144:147], v[236:239], v[156:159], v[0:3]
	v_mfma_f32_16x16x32_f16 v[0:3], v[104:107], v[188:191], v[80:83]
	v_mfma_f32_16x16x32_f16 v[80:83], v[108:111], v[192:195], v[0:3]
	v_mfma_f32_16x16x32_f16 v[0:3], v[116:119], v[188:191], v[84:87]
	v_mfma_f32_16x16x32_f16 v[148:151], v[236:239], v[192:195], v[0:3]
	v_mfma_f32_16x16x32_f16 v[0:3], v[104:107], v[196:199], v[88:91]
	v_mfma_f32_16x16x32_f16 v[152:155], v[108:111], v[200:203], v[0:3]
	v_mfma_f32_16x16x32_f16 v[0:3], v[116:119], v[196:199], v[92:95]
	v_mfma_f32_16x16x32_f16 v[156:159], v[236:239], v[200:203], v[0:3]
	s_setprio 0
	s_add_i32 s49, s49, s17
	s_cmpk_lt_i32 s49, 0x1c8
	s_cselect_b64 s[6:7], -1, 0
	s_cmpk_gt_i32 s49, 0x1c7
	s_cselect_b64 s[12:13], -1, 0
	s_and_b64 vcc, exec, s[12:13]
	s_mov_b32 s54, s2
	s_mov_b32 s53, s51
	s_mov_b32 s55, s52
	s_barrier
	s_cbranch_vccnz .LBB1_100
	s_cmpk_lt_i32 s49, 0x148
	s_cbranch_scc1 .LBB1_88
	s_cmpk_lt_u32 s49, 0x1a0
	s_cbranch_scc1 .LBB1_89
	s_cmpk_lt_u32 s49, 0x1b8
	s_cbranch_scc1 .LBB1_90
	s_cmpk_lt_u32 s49, 0x1c0
	s_cselect_b32 s47, s45, 0xfffffe40
	s_cselect_b32 s48, 3, 4
	s_mov_b32 s3, 1
	s_cmp_lt_i32 s48, 1
	s_movk_i32 s53, 0x64
	s_cbranch_scc0 .LBB1_91
	s_branch .LBB1_99

.LBB2_36:
	s_waitcnt lgkmcnt(0)
	s_cmpk_lt_u32 s37, 0x1c8
	s_cselect_b32 s57, s13, s17
	s_cselect_b32 s56, s12, s16
	s_cselect_b32 s59, s15, s19
	s_cselect_b32 s58, s14, s18
	v_lshlrev_b32_e32 v106, 2, v0
	global_load_dword v107, v106, s[56:57]
	global_load_dword v106, v106, s[58:59]
	v_lshrrev_b32_e32 v2, 4, v0
	v_and_b32_e32 v1, 15, v0
	v_mov_b32_e32 v5, 0
	v_cmp_gt_u32_e32 vcc, s41, v1
	v_lshlrev_b32_e32 v2, 3, v2
	v_mov_b32_e32 v4, v5
	s_and_saveexec_b64 s[42:43], vcc
	s_cbranch_execz .LBB2_40
	s_mul_i32 s49, s41, s44
	s_mul_i32 s50, s35, 0x1c8
	v_mov_b32_e32 v3, 0
	s_waitcnt lgkmcnt(0)
	v_lshl_add_u64 v[6:7], s[8:9], 0, v[2:3]
	s_add_i32 s8, s49, s50
	s_add_i32 s48, s8, s48
	s_mov_b64 s[8:9], 0
	v_mov_b32_e32 v10, v1
	v_mov_b32_e32 v4, v3
	v_mov_b32_e32 v5, v3
.LBB2_38:
	v_add_u32_e32 v12, s48, v10
	v_ashrrev_i32_e32 v13, 31, v12
	v_lshlrev_b64 v[12:13], 8, v[12:13]
	v_lshl_add_u64 v[12:13], v[6:7], 0, v[12:13]
	global_load_dwordx2 v[14:15], v[12:13], off
	global_load_dwordx2 v[16:17], v[12:13], off offset:128
	v_mov_b32_e32 v94, 0
	v_mov_b32_e32 v95, 0
	v_mov_b32_e32 v96, 0
	v_mov_b32_e32 v97, 0
	v_mov_b32_e32 v98, 0
	v_mov_b32_e32 v99, 0
	v_mov_b32_e32 v100, 0
	v_mov_b32_e32 v101, 0
	s_mov_b64 s[52:53], 0x1000
	s_mov_b64 s[54:55], exec
	v_add_u32_e32 v102, 16, v10
	v_cmp_gt_u32_e32 vcc, s41, v102
	s_and_b64 exec, exec, vcc
	v_lshl_add_u64 v[104:105], s[52:53], 0, v[12:13]
	global_load_dwordx2 v[94:95], v[104:105], off
	global_load_dwordx2 v[96:97], v[104:105], off offset:128
	v_add_u32_e32 v102, 32, v10
	v_cmp_gt_u32_e32 vcc, s41, v102
	s_and_b64 exec, exec, vcc
	v_lshl_add_u64 v[104:105], s[52:53], 0, v[104:105]
	global_load_dwordx2 v[98:99], v[104:105], off
	global_load_dwordx2 v[100:101], v[104:105], off offset:128
	s_mov_b64 exec, s[54:55]
	s_waitcnt vmcnt(0)
	v_pk_add_f32 v[12:13], v[14:15], v[16:17]
	v_pk_add_f32 v[94:95], v[94:95], v[96:97]
	v_pk_add_f32 v[98:99], v[98:99], v[100:101]
	v_pk_add_f32 v[4:5], v[4:5], v[12:13]
	s_nop 0
	v_pk_add_f32 v[4:5], v[4:5], v[94:95]
	s_nop 0
	v_pk_add_f32 v[4:5], v[4:5], v[98:99]

.LBB2_53:
	s_or_b64 exec, exec, s[38:39]
	s_addk_i32 s37, 0x1c7
	s_cmpk_lt_u32 s37, 0x38f
	s_cselect_b64 s[42:43], -1, 0
	s_cmpk_gt_u32 s37, 0x38e
	s_cselect_b64 s[38:39], -1, 0
	v_mov_b32_e32 v1, 0
	s_waitcnt lgkmcnt(0)
	s_barrier
	s_and_saveexec_b64 s[8:9], s[6:7]
	s_xor_b64 s[6:7], exec, s[8:9]
	s_or_saveexec_b64 s[6:7], s[6:7]
	v_lshrrev_b32_e32 v5, 1, v0
	v_lshlrev_b32_e32 v4, 1, v0
	s_xor_b64 exec, exec, s[6:7]
	s_cbranch_execz .LBB2_55
	v_mov_b32_e32 v3, v107
	v_mov_b32_e32 v2, v106
	s_movk_i32 s8, 0xfc
	v_bitop3_b32 v6, v5, s8, 4 bitop3:0xc8
	ds_read_b32 v6, v6 offset:49024
	v_and_b32_e32 v7, 0x78, v5
	ds_read_b32 v7, v7 offset:49024
	s_waitcnt vmcnt(0) lgkmcnt(1)
	v_mul_f32_e32 v10, v6, v3
	v_fma_mixlo_f16 v3, v6, v3, 0
	ds_write_b16 v4, v3 offset:48000
	s_waitcnt vmcnt(0) lgkmcnt(1)
	v_fma_mixlo_f16 v2, -v7, v10, v2
	ds_write_b16 v4, v2 offset:48512
